# speedup vs baseline: 1.0667x; 1.0667x over previous
_Z6mainK2PKDF16_S0_S0_PKfPKiS4_S2_PfS0_S4_S4_:
	s_load_dwordx2 s[20:21], s[0:1], 0x50
	s_load_dwordx2 s[24:25], s[0:1], 0x40
	s_load_dwordx2 s[58:59], s[0:1], 0x8
	s_load_dwordx2 s[90:91], s[0:1], 0x28
	v_readfirstlane_b32 s3, v0
	s_lshr_b32 s38, s3, 6
	s_lshl_b32 s2, s2, 3
	s_add_i32 s6, s38, s2
	s_cmpk_lt_i32 s6, 0x753
	v_and_b32_e32 v115, 15, v0
	v_mov_b32_e32 v106, -1
	s_cselect_b64 s[2:3], -1, 0
	s_cmpk_gt_i32 s6, 0x752
	v_mov_b32_e32 v108, -1
	s_cbranch_scc1 .LBB2_2
	s_load_dwordx2 s[4:5], s[0:1], 0x48
	v_lshl_or_b32 v2, s6, 4, v115
	v_ashrrev_i32_e32 v3, 31, v2
	s_waitcnt lgkmcnt(0)
	v_lshl_add_u64 v[2:3], v[2:3], 2, s[4:5]
	global_load_dword v108, v[2:3], off

.LBB2_58:
	v_mov_b32_e32 v187, 0x4138aa3b
	v_lshrrev_b32_e32 v38, 3, v115
	v_lshlrev_b32_e32 v40, 5, v0
	v_lshrrev_b32_e32 v107, 4, v110
	s_lshl_b32 s6, s38, 13
	v_and_or_b32 v38, v175, 2, v38
	v_and_b32_e32 v40, 0x180, v40
	v_lshlrev_b32_e32 v41, 3, v0
	s_add_i32 s6, s6, 0x12000
	v_lshlrev_b32_e32 v39, 9, v107
	v_and_or_b32 v40, v41, 24, v40
	v_lshlrev_b32_e32 v38, 5, v38
	v_lshrrev_b32_e32 v37, 3, v0
	v_or3_b32 v39, v40, v39, s6
	v_xor_b32_e32 v40, 32, v38
	v_lshl_add_u32 v191, v110, 5, s39
	v_and_b32_e32 v0, 7, v0
	v_or_b32_e32 v186, v39, v38
	v_or_b32_e32 v188, v39, v40
	v_xor_b32_e32 v40, 64, v38
	v_xor_b32_e32 v38, 0x60, v38
	v_bitop3_b32 v0, v37, v0, 6 bitop3:0x6c
	v_or_b32_e32 v190, v39, v38
	v_and_b32_e32 v1, 0x380, v122
	v_lshlrev_b32_e32 v38, 4, v0
	v_add_u32_e32 v0, s33, v115
	v_or_b32_e32 v189, v39, v40
	v_lshlrev_b32_e32 v34, 2, v34
	v_mov_b32_e32 v35, 0
	v_and_b32_e32 v122, 6, v115
	v_xor_b32_e32 v122, v122, v107
	v_lshlrev_b32_e32 v122, 4, v122
	v_lshl_add_u32 v122, v115, 7, v122
	v_add_u32_e32 v122, s6, v122
	s_mov_b32 s60, 0xffff0000
	s_mov_b32 s61, 0
	s_mov_b32 s62, 0
	s_mov_b32 s63, 0xffff
	s_mov_b32 s64, 0
	s_mov_b32 s65, 0xffff0000
	v_or_b32_e32 v39, s6, v1
	v_add_u32_e32 v192, 0x15f90, v0
	v_lshlrev_b32_e32 v0, 7, v107
	v_and_b32_e32 v1, 0x78, v41
	v_lshl_add_u64 v[126:127], s[30:31], 0, v[34:35]
	v_or3_b32 v193, v1, v0, s39
	v_add_u32_e32 v0, s33, v110
	v_mov_b32_e32 v34, v116
	v_mov_b32_e32 v37, v35
	v_lshl_or_b32 v194, v110, 16, v0
	v_lshl_add_u64 v[0:1], v[34:35], 0, v[36:37]
	v_mov_b32_e32 v36, v35
	v_mov_b32_e32 v76, v35
	v_mov_b32_e32 v77, v35
	v_lshl_add_u64 v[0:1], s[34:35], 0, v[0:1]
	v_mov_b32_e32 v34, v35
	v_mov_b32_e32 v74, v35
	v_mov_b32_e32 v75, v35
	s_mov_b32 s12, 0x3c003c00
	v_mov_b64_e32 v[80:81], v[76:77]
	v_mov_b64_e32 v[84:85], v[76:77]
	v_mov_b64_e32 v[88:89], v[76:77]
	v_mov_b64_e32 v[92:93], v[76:77]
	v_mov_b64_e32 v[96:97], v[76:77]
	v_mov_b64_e32 v[100:101], v[76:77]
	v_mov_b64_e32 v[104:105], v[76:77]
	v_mov_b64_e32 v[56:57], v[36:37]
	v_mov_b64_e32 v[60:61], v[36:37]
	v_mov_b64_e32 v[64:65], v[36:37]
	v_mov_b64_e32 v[68:69], v[36:37]
	v_mov_b64_e32 v[72:73], v[36:37]
	s_or_b32 s47, s40, 0x80
	v_lshl_add_u64 v[0:1], v[0:1], 0, 64
	s_mov_b32 s49, 0
	s_mov_b64 s[30:31], -1
	s_mov_b32 s13, s12
	s_movk_i32 s48, 0x300
	v_lshl_add_u32 v118, v114, 2, v116
	v_mov_b32_e32 v116, 0xc3500
	v_lshlrev_b32_e32 v128, 2, v114
	v_add_u32_e32 v196, v39, v38
	v_mov_b64_e32 v[78:79], v[74:75]
	v_mov_b64_e32 v[82:83], v[74:75]
	v_mov_b64_e32 v[86:87], v[74:75]
	v_mov_b64_e32 v[90:91], v[74:75]
	v_mov_b64_e32 v[94:95], v[74:75]
	v_mov_b64_e32 v[98:99], v[74:75]
	v_mov_b64_e32 v[102:103], v[74:75]
	v_mov_b64_e32 v[54:55], v[34:35]
	v_mov_b64_e32 v[58:59], v[34:35]
	v_mov_b64_e32 v[62:63], v[34:35]
	v_mov_b64_e32 v[66:67], v[34:35]
	v_mov_b32_e32 v197, 0
	s_mov_b32 s50, 0
	v_mov_b64_e32 v[70:71], v[34:35]
	v_mov_b32_e32 v50, v35
	v_mov_b32_e32 v51, v35
	v_mov_b32_e32 v52, v35
	v_mov_b32_e32 v53, v35
	v_mov_b32_e32 v46, v35
	v_mov_b32_e32 v47, v35
	v_mov_b32_e32 v48, v35
	v_mov_b32_e32 v49, v35
	v_mov_b32_e32 v42, v35
	v_mov_b32_e32 v43, v35
	v_mov_b32_e32 v44, v35
	v_mov_b32_e32 v45, v35
	v_mov_b32_e32 v38, v35
	v_mov_b32_e32 v39, v35
	v_mov_b32_e32 v40, v35
	v_mov_b32_e32 v41, v35
	s_waitcnt vmcnt(0)
	ds_write_b128 v196, v[10:13]
	ds_write_b128 v196, v[14:17] offset:1024
	ds_write_b128 v196, v[30:33] offset:2048
	ds_write_b128 v196, v[26:29] offset:3072
	ds_write_b128 v196, v[2:5] offset:4096
	ds_write_b128 v196, v[6:9] offset:5120
	ds_write_b128 v196, v[18:21] offset:6144
	ds_write_b128 v196, v[22:25] offset:7168
	s_mul_i32 s78, s42, 0xc00
	s_add_i32 s78, s78, s40
	s_lshl_b32 s6, s43, 6
	s_sub_i32 s83, s44, s6
	s_lshl_b32 s6, s43, 8
	s_add_i32 s82, s78, s6
	v_add_u32_e32 v229, s82, v172
	v_add_u32_e32 v230, s82, v173
	ds_read_u16 v224, v229 offset:0
	ds_read_u16 v225, v229 offset:32
	ds_read_u16 v226, v229 offset:64
	ds_read_u16 v227, v229 offset:96
	ds_read_u16 v232, v229 offset:128
	ds_read_u16 v233, v229 offset:160
	ds_read_u16 v234, v229 offset:192
	ds_read_u16 v235, v229 offset:224
	ds_read_b32 v198, v230
	s_waitcnt lgkmcnt(0)
	s_mov_b32 s77, 1
	s_branch .Lmk_gather

.LBB2_64:
	s_mov_b64 s[54:55], s[6:7]
	s_lshl_b32 s66, s49, 6
	s_sub_i32 s66, s41, s66
	s_cmp_gt_i32 s66, 32
	s_cselect_b64 s[80:81], -1, 0
	v_bfe_u32 v34, v121, 16, 4
	v_cmp_gt_i32_e64 s[56:57], s66, v110
	v_lshl_add_u32 v115, v34, 1, v191
	v_lshlrev_b32_e32 v34, 2, v34
	ds_bpermute_b32 v121, v34, v197
	v_xor_b32_e32 v34, 64, v122
	ds_read_b128 v[208:211], v122
	ds_read_b128 v[212:215], v34
	ds_read_b128 v[216:219], v122 offset:2048
	ds_read_b128 v[220:223], v34 offset:2048
	ds_read_b128 v[224:227], v122 offset:4096
	ds_read_b128 v[228:231], v34 offset:4096
	ds_read_b128 v[232:235], v122 offset:6144
	ds_read_b128 v[236:239], v34 offset:6144
	ds_read_b64_tr_b16 v[130:131], v186 offset:0
	ds_read_b64_tr_b16 v[132:133], v186 offset:2048
	ds_read_b64_tr_b16 v[134:135], v188 offset:0
	ds_read_b64_tr_b16 v[136:137], v188 offset:2048
	ds_read_b64_tr_b16 v[138:139], v189 offset:0
	ds_read_b64_tr_b16 v[140:141], v189 offset:2048
	ds_read_b64_tr_b16 v[142:143], v190 offset:0
	ds_read_b64_tr_b16 v[144:145], v190 offset:2048
	s_waitcnt vmcnt(8)
.Lmk_ua_ready:
	s_waitcnt lgkmcnt(8)
	v_mfma_f32_16x16x32_f16 v[200:203], v[240:243], v[208:211], 0
	v_mfma_f32_16x16x32_f16 v[160:163], v[240:243], v[216:219], 0
	v_mfma_f32_16x16x32_f16 v[248:251], v[240:243], v[224:227], 0
	v_mfma_f32_16x16x32_f16 v[252:255], v[240:243], v[232:235], 0
	v_mfma_f32_16x16x32_f16 v[200:203], v[244:247], v[212:215], v[200:203]
	v_mfma_f32_16x16x32_f16 v[160:163], v[244:247], v[220:223], v[160:163]
	v_mfma_f32_16x16x32_f16 v[248:251], v[244:247], v[228:231], v[248:251]
	v_mfma_f32_16x16x32_f16 v[252:255], v[244:247], v[236:239], v[252:255]
	ds_read_b64_tr_b16 v[146:147], v186 offset:4096
	ds_read_b64_tr_b16 v[148:149], v186 offset:6144
	ds_read_b64_tr_b16 v[150:151], v188 offset:4096
	ds_read_b64_tr_b16 v[152:153], v188 offset:6144
	ds_read_b64_tr_b16 v[154:155], v189 offset:4096
	ds_read_b64_tr_b16 v[156:157], v189 offset:6144
	ds_read_b64_tr_b16 v[204:205], v190 offset:4096
	ds_read_b64_tr_b16 v[206:207], v190 offset:6144
	v_cndmask_b32_e64 v34, v200, v160, s[60:61]
	v_cndmask_b32_e64 v34, v34, v248, s[62:63]
	v_cndmask_b32_e64 v34, v34, v252, s[64:65]
	v_cndmask_b32_e64 v201, v195, v185, s[54:55]
	v_add_f32_e32 v202, 0x40200000, v201
	v_add_f32_e32 v34, v34, v121
	v_mul_f32_e32 v121, 0x3e4ccccd, v34
	v_max_f32_e32 v34, v34, v121
	v_cmp_gt_f32_e32 vcc, v34, v202
	s_and_b64 s[68:69], s[56:57], vcc
	s_cmp_eq_u64 s[68:69], 0
	s_cbranch_scc1 .Lmk_nomax_pre
	v_cndmask_b32_e64 v161, v185, v34, s[56:57]
	s_lshl_b32 s6, s43, 6
	s_sub_i32 s83, s44, s6
	v_max_f32_dpp v161, v161, v161 row_shr:1 row_mask:0xf bank_mask:0xf
	s_lshl_b32 s6, s43, 8
	s_add_i32 s82, s78, s6
	v_max_f32_dpp v161, v161, v161 row_shr:2 row_mask:0xf bank_mask:0xf
	v_add_u32_e32 v229, s82, v172
	v_add_u32_e32 v230, s82, v173
	v_max_f32_dpp v161, v161, v161 row_shr:4 row_mask:0xf bank_mask:0xf
	ds_read_u16 v224, v229 offset:0
	ds_read_u16 v225, v229 offset:32
	v_max_f32_dpp v161, v161, v161 row_shr:8 row_mask:0xf bank_mask:0xf
	ds_read_u16 v226, v229 offset:64
	ds_read_u16 v227, v229 offset:96
	v_max_f32_dpp v161, v161, v161 row_bcast:15 row_mask:0xa bank_mask:0xf
	ds_read_u16 v232, v229 offset:128
	ds_read_u16 v233, v229 offset:160
	v_max_f32_dpp v161, v161, v161 row_bcast:31 row_mask:0xc bank_mask:0xf
	ds_read_u16 v234, v229 offset:192
	ds_read_u16 v235, v229 offset:224
	v_readlane_b32 s70, v161, 63
	ds_read_b32 v198, v230
	v_mov_b64_e32 v[208:209], s[12:13]
	v_mov_b64_e32 v[210:211], s[12:13]
	s_and_b64 vcc, exec, s[54:55]
	s_nop 0
	v_mov_b32_e32 v161, s70
	s_cbranch_vccnz .Lmk_norescale
	v_sub_f32_e32 v162, v195, v161
	v_mul_f32_e32 v162, 0x3fb8aa3b, v162
	v_exp_f32_e32 v248, v162
	s_nop 0
	v_pk_mul_f32 v[56:57], v[248:249], v[56:57] op_sel_hi:[0,1]
	v_pk_mul_f32 v[54:55], v[248:249], v[54:55] op_sel_hi:[0,1]
	v_pk_mul_f32 v[60:61], v[248:249], v[60:61] op_sel_hi:[0,1]
	v_pk_mul_f32 v[58:59], v[248:249], v[58:59] op_sel_hi:[0,1]
	v_pk_mul_f32 v[64:65], v[248:249], v[64:65] op_sel_hi:[0,1]
	v_pk_mul_f32 v[62:63], v[248:249], v[62:63] op_sel_hi:[0,1]
	v_pk_mul_f32 v[68:69], v[248:249], v[68:69] op_sel_hi:[0,1]
	v_pk_mul_f32 v[66:67], v[248:249], v[66:67] op_sel_hi:[0,1]
	v_pk_mul_f32 v[72:73], v[72:73], v[248:249] op_sel_hi:[1,0]
	v_pk_mul_f32 v[70:71], v[70:71], v[248:249] op_sel_hi:[1,0]

.Lmk_nomax_pre:
	s_lshl_b32 s6, s43, 6
	s_sub_i32 s83, s44, s6
	s_lshl_b32 s6, s43, 8
	s_add_i32 s82, s78, s6
	v_add_u32_e32 v229, s82, v172
	v_add_u32_e32 v230, s82, v173
	ds_read_u16 v224, v229 offset:0
	ds_read_u16 v225, v229 offset:32
	ds_read_u16 v226, v229 offset:64
	ds_read_u16 v227, v229 offset:96
	ds_read_u16 v232, v229 offset:128
	ds_read_u16 v233, v229 offset:160
	ds_read_u16 v234, v229 offset:192
	ds_read_u16 v235, v229 offset:224
	ds_read_b32 v198, v230
	v_mov_b64_e32 v[208:209], s[12:13]
	v_mov_b64_e32 v[210:211], s[12:13]
.Lmk_nomax:
	v_mov_b32_e32 v195, v201
	v_sub_f32_e32 v34, v34, v195
	v_fmamk_f32 v34, v34, 0x3fb8aa3b, v187
	v_exp_f32_e32 v34, v34
	s_nop 0
	v_cvt_f16_f32_e32 v34, v34
	v_cndmask_b32_e64 v34, 0, v34, s[56:57]
	ds_write_b16 v115, v34
	ds_read_b64_tr_b16 v[200:201], v193 offset:0
	ds_read_b64_tr_b16 v[202:203], v193 offset:512
	ds_read_b64_tr_b16 v[160:161], v193 offset:1024
	ds_read_b64_tr_b16 v[162:163], v193 offset:1536
	s_and_b64 vcc, exec, s[54:55]
	s_cbranch_vccnz .Lmk_first_path
	s_waitcnt vmcnt(0)
	s_waitcnt lgkmcnt(0)
	v_mfma_f32_16x16x32_f16 v[54:57], v[130:133], v[200:203], v[54:57]
	ds_write_b16 v115, v35
	ds_write_b128 v196, v[10:13]
	v_mfma_f32_16x16x32_f16 v[58:61], v[134:137], v[200:203], v[58:61]
	ds_write_b128 v196, v[14:17] offset:1024
	v_mfma_f32_16x16x32_f16 v[62:65], v[138:141], v[200:203], v[62:65]
	ds_write_b128 v196, v[30:33] offset:2048
	v_mfma_f32_16x16x32_f16 v[66:69], v[142:145], v[200:203], v[66:69]
	ds_write_b128 v196, v[26:29] offset:3072
	v_mfma_f32_16x16x32_f16 v[70:73], v[208:211], v[200:203], v[70:73]

.LBB2_76:
	s_and_b64 vcc, exec, s[54:55]
	s_cbranch_vccz .LBB2_110
	s_cmp_gt_i32 s50, 35
	s_cbranch_scc1 .LBB2_110
	s_add_i32 s36, s50, 2
	s_mul_hi_i32 s0, s36, 0x55555556
	s_lshr_b32 s1, s0, 31
	s_add_i32 s0, s0, s1
	s_mul_i32 s0, s0, 3
	s_sub_i32 s37, s36, s0
	s_mulk_i32 s37, 0xc00
	s_add_i32 s38, s40, s37
	v_add_u32_e32 v36, v129, v114
	s_and_saveexec_b64 s[0:1], s[4:5]
	v_lshl_add_u32 v37, v110, 2, s38
	ds_write_b32 v37, v194
	s_or_b64 exec, exec, s[0:1]
	v_lshl_add_u32 v37, v36, 2, s38
	s_waitcnt vmcnt(8)
	v_cmp_lt_i32_e32 vcc, v114, v169
	s_and_saveexec_b64 s[0:1], vcc
	ds_write_b32 v37, v125 offset:64
	s_or_b64 exec, exec, s[0:1]
	v_cmp_lt_i32_e32 vcc, v109, v169
	s_and_saveexec_b64 s[0:1], vcc
	ds_write_b32 v37, v117 offset:80
	s_or_b64 exec, exec, s[0:1]
	v_cmp_lt_i32_e32 vcc, v123, v169
	s_and_saveexec_b64 s[0:1], vcc
	ds_write_b32 v37, v171 offset:96
	s_or_b64 exec, exec, s[0:1]
	v_cmp_lt_i32_e32 vcc, v164, v169
	s_and_saveexec_b64 s[0:1], vcc
	ds_write_b32 v37, v170 offset:112
	s_or_b64 exec, exec, s[0:1]
	v_cmp_lt_i32_e32 vcc, v165, v169
	s_and_saveexec_b64 s[0:1], vcc
	s_cbranch_execz .LBB2_109
	v_ashrrev_i32_e32 v121, 31, v120
	s_add_i32 s37, s47, s37
	v_lshl_add_u32 v130, v36, 2, s37
	v_lshlrev_b64 v[36:37], 2, v[120:121]
	v_mad_i64_i32 v[36:37], s[36:37], s36, v116, v[36:37]
	v_lshl_add_u64 v[36:37], v[0:1], 0, v[36:37]
	s_mov_b64 s[36:37], 0
	v_mov_b32_e32 v121, v165
	s_branch .LBB2_91

.LBB2_110:
	s_add_i32 s11, s50, 2
	s_cmp_eq_u32 s42, s11
	s_cbranch_scc1 .Lmk_reread
.Lmk_gather:
	s_cmp_gt_i32 s83, 32
	v_lshl_or_b32 v10, v224, 7, v176
	v_lshl_or_b32 v14, v225, 7, v176
	s_cselect_b64 s[30:31], -1, 0
	v_lshl_or_b32 v30, v226, 7, v176
	v_lshl_or_b32 v26, v227, 7, v176
	s_cmp_lt_i32 s83, 33
	global_load_dwordx4 v[10:13], v10, s[28:29]
	global_load_dwordx4 v[14:17], v14, s[28:29]
	global_load_dwordx4 v[30:33], v30, s[28:29]
	global_load_dwordx4 v[26:29], v26, s[28:29]
	s_cbranch_scc1 .LBB2_68
	v_lshl_or_b32 v2, v232, 7, v176
	v_lshl_or_b32 v6, v233, 7, v176
	v_lshl_or_b32 v18, v234, 7, v176
	v_lshl_or_b32 v22, v235, 7, v176
	global_load_dwordx4 v[2:5], v2, s[28:29]
	global_load_dwordx4 v[6:9], v6, s[28:29]
	global_load_dwordx4 v[18:21], v18, s[28:29]
	global_load_dwordx4 v[22:25], v22, s[28:29]

.Lmk_ma_ready:
	s_nop 0
	v_rcp_f32_e32 v36, v70
	s_nop 0
	v_fma_f32 v37, -v70, v36, 2.0
	v_mul_f32_e32 v36, v36, v37
	v_pk_mul_f32 v[200:201], v[36:37], v[54:55] op_sel_hi:[0,1]
	v_pk_mul_f32 v[202:203], v[36:37], v[56:57] op_sel_hi:[0,1]
	v_pk_mul_f32 v[160:161], v[36:37], v[58:59] op_sel_hi:[0,1]
	v_pk_mul_f32 v[162:163], v[36:37], v[60:61] op_sel_hi:[0,1]
	v_cvt_pk_f16_f32 v130, v200, v201
	v_cvt_pk_f16_f32 v131, v202, v203
	v_cvt_pk_f16_f32 v132, v160, v161
	v_cvt_pk_f16_f32 v133, v162, v163
	v_pk_mul_f32 v[200:201], v[36:37], v[62:63] op_sel_hi:[0,1]
	v_pk_mul_f32 v[202:203], v[36:37], v[64:65] op_sel_hi:[0,1]
	v_pk_mul_f32 v[160:161], v[36:37], v[66:67] op_sel_hi:[0,1]
	v_pk_mul_f32 v[162:163], v[36:37], v[68:69] op_sel_hi:[0,1]
	v_cvt_pk_f16_f32 v134, v200, v201
	v_cvt_pk_f16_f32 v135, v202, v203
	v_cvt_pk_f16_f32 v136, v160, v161
	v_cvt_pk_f16_f32 v137, v162, v163
	v_mfma_f32_16x16x32_f16 v[50:53], v[86:89], v[130:133], v[50:53]
	v_mfma_f32_16x16x32_f16 v[46:49], v[78:81], v[130:133], v[46:49]
	v_mfma_f32_16x16x32_f16 v[42:45], v[90:93], v[130:133], v[42:45]
	v_mfma_f32_16x16x32_f16 v[38:41], v[98:101], v[130:133], v[38:41]
	v_mfma_f32_16x16x32_f16 v[50:53], v[82:85], v[134:137], v[50:53]
	v_mfma_f32_16x16x32_f16 v[46:49], v[74:77], v[134:137], v[46:49]
	v_mfma_f32_16x16x32_f16 v[42:45], v[94:97], v[134:137], v[42:45]
	v_mfma_f32_16x16x32_f16 v[38:41], v[102:105], v[134:137], v[38:41]

.Lmk_first_path:
	s_waitcnt vmcnt(10)
	s_waitcnt lgkmcnt(0)
	v_mfma_f32_16x16x32_f16 v[54:57], v[130:133], v[200:203], 0
	ds_write_b16 v115, v35
	ds_write_b128 v196, v[10:13]
	v_mfma_f32_16x16x32_f16 v[58:61], v[134:137], v[200:203], 0
	ds_write_b128 v196, v[14:17] offset:1024
	v_mfma_f32_16x16x32_f16 v[62:65], v[138:141], v[200:203], 0
	ds_write_b128 v196, v[30:33] offset:2048
	v_mfma_f32_16x16x32_f16 v[66:69], v[142:145], v[200:203], 0
	ds_write_b128 v196, v[26:29] offset:3072
	v_mfma_f32_16x16x32_f16 v[70:73], v[208:211], v[200:203], 0
	s_branch .Lmk_agg_join
.Lmk_reread:
	s_and_b64 vcc, exec, s[54:55]
	s_cbranch_vccz .Lmk_gather
	s_lshl_b32 s6, s43, 6
	s_sub_i32 s83, s44, s6
	s_lshl_b32 s6, s43, 8
	s_add_i32 s82, s78, s6
	v_add_u32_e32 v229, s82, v172
	v_add_u32_e32 v230, s82, v173
	ds_read_u16 v224, v229 offset:0
	ds_read_u16 v225, v229 offset:32
	ds_read_u16 v226, v229 offset:64
	ds_read_u16 v227, v229 offset:96
	ds_read_u16 v232, v229 offset:128
	ds_read_u16 v233, v229 offset:160
	ds_read_u16 v234, v229 offset:192
	ds_read_u16 v235, v229 offset:224
	ds_read_b32 v198, v230
	s_waitcnt lgkmcnt(0)
	s_branch .Lmk_gather
.LBB2_93:
	v_lshlrev_b32_e32 v36, 4, v107
	v_lshl_or_b32 v36, s50, 8, v36
	global_load_dwordx4 v[240:243], v36, s[58:59]
	global_load_dwordx4 v[244:247], v36, s[58:59] offset:64
	s_cmp_gt_i32 s50, 35
	v_mov_b32_e32 v169, 0
	s_cbranch_scc1 .LBB2_103
	v_sub_u32_e32 v169, v174, v124
	s_add_i32 s0, s50, 2
	v_mov_b32_e32 v74, 0
	v_cndmask_b32_e64 v34, 0, v169, s[2:3]
	s_mul_i32 s0, s0, 0xc3500
	v_lshl_add_u32 v36, v124, 2, v118
	v_add_u32_dpp v34, v34, v34 row_shr:1 row_mask:0xf bank_mask:0xf bound_ctrl:1
	s_add_u32 s0, s90, s0
	s_addc_u32 s1, s91, 0
	v_add_u32_dpp v34, v34, v34 row_shr:2 row_mask:0xf bank_mask:0xf bound_ctrl:1
	v_mov_b32_e32 v120, v124
	s_nop 0
	v_add_u32_dpp v34, v34, v34 row_shr:4 row_mask:0xf bank_mask:0xf bound_ctrl:1
	global_load_dword v125, v36, s[0:1]
	global_load_dword v117, v36, s[0:1] offset:16
	v_add_u32_dpp v34, v34, v34 row_shr:8 row_mask:0xf bank_mask:0xf bound_ctrl:1
	global_load_dword v171, v36, s[0:1] offset:32
	global_load_dword v170, v36, s[0:1] offset:48
	v_add_u32_dpp v34, v34, v34 row_bcast:15 row_mask:0xa bank_mask:0xf
	s_nop 1
	v_mov_b32_dpp v74, v34 row_bcast:31 row_mask:0xc bank_mask:0xf
	v_sub_u32_e32 v36, v74, v169
	v_add_u32_e32 v129, v36, v34
	v_sub_u32_e32 v36, 0x2f0, v129
	v_min_i32_e32 v169, v169, v36
.LBB2_103:
	s_cmp_gt_i32 s50, 34
	s_cbranch_scc1 .LBB2_105
	s_add_i32 s0, s50, 3
	s_add_u32 s10, s26, s0
	s_addc_u32 s11, s27, 0
	s_lshl_b64 s[10:11], s[10:11], 6
	v_lshl_add_u64 v[36:37], v[126:127], 0, s[10:11]
	global_load_dword v124, v[36:37], off
	global_load_dword v174, v[36:37], off offset:2432
.LBB2_105:
	s_lshl_b32 s0, s50, 13
	v_lshl_add_u32 v36, v110, 4, s0
	v_mov_b32_e32 v197, v184
	global_load_dwordx4 v[86:89], v36, s[16:17]
	global_load_dwordx4 v[82:85], v36, s[16:17] offset:1024
	global_load_dwordx4 v[78:81], v36, s[16:17] offset:2048
	global_load_dwordx4 v[74:77], v36, s[16:17] offset:3072
	v_add_u32_e32 v37, 0x1000, v36
	v_cvt_f32_f16_e32 v184, v199
	global_load_dwordx4 v[90:93], v37, s[16:17]
	global_load_dwordx4 v[94:97], v37, s[16:17] offset:1024
	global_load_dwordx4 v[98:101], v37, s[16:17] offset:2048
	global_load_dwordx4 v[102:105], v37, s[16:17] offset:3072
	s_cmp_gt_u32 s50, 35
	s_cbranch_scc1 .LBB2_64
	s_mul_i32 s0, s50, 0x1d4c0
	s_add_i32 s0, s0, 0x1d4c0
	v_lshl_add_u32 v34, v192, 1, s0
	global_load_ushort v199, v34, s[24:25]
	s_branch .LBB2_64
